# window-attention block epilogue: O transposed through a private LDS tile per wave, 8 row-contiguous 16-byte stores instead of 64 shuffle+4-byte-store steps
# speedup vs baseline: 1.0116x; 1.0009x over previous
.LBB0_635:
	s_waitcnt vmcnt(8)
	s_waitcnt vmcnt(9)
	ds_write_b128 v221, v[98:101] offset:32768
	s_waitcnt vmcnt(8)
	ds_write_b128 v221, v[102:105] offset:40960
	s_and_saveexec_b64 s[8:9], s[4:5]
	ds_write_b32 v223, v114
	s_or_b64 exec, exec, s[8:9]
	s_waitcnt lgkmcnt(0)
	ds_read_b128 v[66:69], v205
	ds_read_b128 v[70:73], v205 offset:32
	ds_read_b128 v[74:77], v205 offset:64
	ds_read_b128 v[78:81], v205 offset:96
	s_add_u32 s0, s22, s24
	s_addc_u32 s1, s23, s25
	s_lshl_b32 s2, s43, 12
	s_add_u32 s0, s0, s2
	s_addc_u32 s1, s1, 0
	v_lshrrev_b32_e32 v82, 6, v254
	v_lshlrev_b32_e32 v82, 13, v82
	v_add_u32_e32 v82, 0x11000, v82
	v_and_b32_e32 v83, 31, v213
	v_lshrrev_b32_e32 v84, 5, v213
	v_lshlrev_b32_e32 v83, 1, v83
	v_lshl_add_u32 v83, v84, 10, v83
	v_add_u32_e32 v83, v82, v83
	v_lshl_add_u32 v82, v213, 4, v82
	v_lshrrev_b32_e32 v84, 4, v213
	v_and_b32_e32 v85, 15, v213
	v_lshlrev_b32_e32 v85, 4, v85
	v_lshl_add_u32 v84, v84, 12, v85
	s_waitcnt lgkmcnt(0)
	v_rcp_f32_e32 v66, v66
	v_rcp_f32_e32 v67, v67
	v_rcp_f32_e32 v68, v68
	v_rcp_f32_e32 v69, v69
	v_rcp_f32_e32 v70, v70
	v_rcp_f32_e32 v71, v71
	v_rcp_f32_e32 v72, v72
	v_rcp_f32_e32 v73, v73
	v_rcp_f32_e32 v74, v74
	v_rcp_f32_e32 v75, v75
	v_rcp_f32_e32 v76, v76
	v_rcp_f32_e32 v77, v77
	v_rcp_f32_e32 v78, v78
	v_rcp_f32_e32 v79, v79
	v_rcp_f32_e32 v80, v80
	v_rcp_f32_e32 v81, v81
	v_mul_f32_e32 v50, v50, v66
	v_mul_f32_e32 v34, v34, v66
	v_mul_f32_e32 v18, v18, v66
	v_mul_f32_e32 v2, v2, v66
	v_mul_f32_e32 v51, v51, v67
	v_mul_f32_e32 v35, v35, v67
	v_mul_f32_e32 v19, v19, v67
	v_mul_f32_e32 v3, v3, v67
	v_mov_b32_dpp v114, v50 quad_perm:[1,0,3,2] row_mask:0xf bank_mask:0xf
	v_mov_b32_dpp v115, v34 quad_perm:[1,0,3,2] row_mask:0xf bank_mask:0xf
	v_mov_b32_dpp v116, v18 quad_perm:[1,0,3,2] row_mask:0xf bank_mask:0xf
	v_mov_b32_dpp v117, v2 quad_perm:[1,0,3,2] row_mask:0xf bank_mask:0xf
	v_mov_b32_dpp v118, v51 quad_perm:[1,0,3,2] row_mask:0xf bank_mask:0xf
	v_mov_b32_dpp v119, v35 quad_perm:[1,0,3,2] row_mask:0xf bank_mask:0xf
	v_mov_b32_dpp v120, v19 quad_perm:[1,0,3,2] row_mask:0xf bank_mask:0xf
	v_mov_b32_dpp v121, v3 quad_perm:[1,0,3,2] row_mask:0xf bank_mask:0xf
	v_cvt_pk_bf16_f32 v50, v50, v114
	v_cvt_pk_bf16_f32 v34, v34, v115
	v_cvt_pk_bf16_f32 v18, v18, v116
	v_cvt_pk_bf16_f32 v2, v2, v117
	v_cvt_pk_bf16_f32 v51, v51, v118
	v_cvt_pk_bf16_f32 v35, v35, v119
	v_cvt_pk_bf16_f32 v19, v19, v120
	v_cvt_pk_bf16_f32 v3, v3, v121
	v_mul_f32_e32 v52, v52, v68
	v_mul_f32_e32 v36, v36, v68
	v_mul_f32_e32 v20, v20, v68
	v_mul_f32_e32 v4, v4, v68
	v_mul_f32_e32 v53, v53, v69
	v_mul_f32_e32 v37, v37, v69
	v_mul_f32_e32 v21, v21, v69
	v_mul_f32_e32 v5, v5, v69
	v_mov_b32_dpp v114, v52 quad_perm:[1,0,3,2] row_mask:0xf bank_mask:0xf
	v_mov_b32_dpp v115, v36 quad_perm:[1,0,3,2] row_mask:0xf bank_mask:0xf
	v_mov_b32_dpp v116, v20 quad_perm:[1,0,3,2] row_mask:0xf bank_mask:0xf
	v_mov_b32_dpp v117, v4 quad_perm:[1,0,3,2] row_mask:0xf bank_mask:0xf
	v_mov_b32_dpp v118, v53 quad_perm:[1,0,3,2] row_mask:0xf bank_mask:0xf
	v_mov_b32_dpp v119, v37 quad_perm:[1,0,3,2] row_mask:0xf bank_mask:0xf
	v_mov_b32_dpp v120, v21 quad_perm:[1,0,3,2] row_mask:0xf bank_mask:0xf
	v_mov_b32_dpp v121, v5 quad_perm:[1,0,3,2] row_mask:0xf bank_mask:0xf
	v_cvt_pk_bf16_f32 v52, v52, v114
	v_cvt_pk_bf16_f32 v36, v36, v115
	v_cvt_pk_bf16_f32 v20, v20, v116
	v_cvt_pk_bf16_f32 v4, v4, v117
	v_cvt_pk_bf16_f32 v53, v53, v118
	v_cvt_pk_bf16_f32 v37, v37, v119
	v_cvt_pk_bf16_f32 v21, v21, v120
	v_cvt_pk_bf16_f32 v5, v5, v121
	v_mul_f32_e32 v54, v54, v70
	v_mul_f32_e32 v38, v38, v70
	v_mul_f32_e32 v22, v22, v70
	v_mul_f32_e32 v6, v6, v70
	v_mul_f32_e32 v55, v55, v71
	v_mul_f32_e32 v39, v39, v71
	v_mul_f32_e32 v23, v23, v71
	v_mul_f32_e32 v7, v7, v71
	v_mov_b32_dpp v114, v54 quad_perm:[1,0,3,2] row_mask:0xf bank_mask:0xf
	v_mov_b32_dpp v115, v38 quad_perm:[1,0,3,2] row_mask:0xf bank_mask:0xf
	v_mov_b32_dpp v116, v22 quad_perm:[1,0,3,2] row_mask:0xf bank_mask:0xf
	v_mov_b32_dpp v117, v6 quad_perm:[1,0,3,2] row_mask:0xf bank_mask:0xf
	v_mov_b32_dpp v118, v55 quad_perm:[1,0,3,2] row_mask:0xf bank_mask:0xf
	v_mov_b32_dpp v119, v39 quad_perm:[1,0,3,2] row_mask:0xf bank_mask:0xf
	v_mov_b32_dpp v120, v23 quad_perm:[1,0,3,2] row_mask:0xf bank_mask:0xf
	v_mov_b32_dpp v121, v7 quad_perm:[1,0,3,2] row_mask:0xf bank_mask:0xf
	v_cvt_pk_bf16_f32 v54, v54, v114
	v_cvt_pk_bf16_f32 v38, v38, v115
	v_cvt_pk_bf16_f32 v22, v22, v116
	v_cvt_pk_bf16_f32 v6, v6, v117
	v_cvt_pk_bf16_f32 v55, v55, v118
	v_cvt_pk_bf16_f32 v39, v39, v119
	v_cvt_pk_bf16_f32 v23, v23, v120
	v_cvt_pk_bf16_f32 v7, v7, v121
	v_mul_f32_e32 v56, v56, v72
	v_mul_f32_e32 v40, v40, v72
	v_mul_f32_e32 v24, v24, v72
	v_mul_f32_e32 v8, v8, v72
	v_mul_f32_e32 v57, v57, v73
	v_mul_f32_e32 v41, v41, v73
	v_mul_f32_e32 v25, v25, v73
	v_mul_f32_e32 v9, v9, v73
	v_mov_b32_dpp v114, v56 quad_perm:[1,0,3,2] row_mask:0xf bank_mask:0xf
	v_mov_b32_dpp v115, v40 quad_perm:[1,0,3,2] row_mask:0xf bank_mask:0xf
	v_mov_b32_dpp v116, v24 quad_perm:[1,0,3,2] row_mask:0xf bank_mask:0xf
	v_mov_b32_dpp v117, v8 quad_perm:[1,0,3,2] row_mask:0xf bank_mask:0xf
	v_mov_b32_dpp v118, v57 quad_perm:[1,0,3,2] row_mask:0xf bank_mask:0xf
	v_mov_b32_dpp v119, v41 quad_perm:[1,0,3,2] row_mask:0xf bank_mask:0xf
	v_mov_b32_dpp v120, v25 quad_perm:[1,0,3,2] row_mask:0xf bank_mask:0xf
	v_mov_b32_dpp v121, v9 quad_perm:[1,0,3,2] row_mask:0xf bank_mask:0xf
	v_cvt_pk_bf16_f32 v56, v56, v114
	v_cvt_pk_bf16_f32 v40, v40, v115
	v_cvt_pk_bf16_f32 v24, v24, v116
	v_cvt_pk_bf16_f32 v8, v8, v117
	v_cvt_pk_bf16_f32 v57, v57, v118
	v_cvt_pk_bf16_f32 v41, v41, v119
	v_cvt_pk_bf16_f32 v25, v25, v120
	v_cvt_pk_bf16_f32 v9, v9, v121
	v_mul_f32_e32 v58, v58, v74
	v_mul_f32_e32 v42, v42, v74
	v_mul_f32_e32 v26, v26, v74
	v_mul_f32_e32 v10, v10, v74
	v_mul_f32_e32 v59, v59, v75
	v_mul_f32_e32 v43, v43, v75
	v_mul_f32_e32 v27, v27, v75
	v_mul_f32_e32 v11, v11, v75
	v_mov_b32_dpp v114, v58 quad_perm:[1,0,3,2] row_mask:0xf bank_mask:0xf
	v_mov_b32_dpp v115, v42 quad_perm:[1,0,3,2] row_mask:0xf bank_mask:0xf
	v_mov_b32_dpp v116, v26 quad_perm:[1,0,3,2] row_mask:0xf bank_mask:0xf
	v_mov_b32_dpp v117, v10 quad_perm:[1,0,3,2] row_mask:0xf bank_mask:0xf
	v_mov_b32_dpp v118, v59 quad_perm:[1,0,3,2] row_mask:0xf bank_mask:0xf
	v_mov_b32_dpp v119, v43 quad_perm:[1,0,3,2] row_mask:0xf bank_mask:0xf
	v_mov_b32_dpp v120, v27 quad_perm:[1,0,3,2] row_mask:0xf bank_mask:0xf
	v_mov_b32_dpp v121, v11 quad_perm:[1,0,3,2] row_mask:0xf bank_mask:0xf
	v_cvt_pk_bf16_f32 v58, v58, v114
	v_cvt_pk_bf16_f32 v42, v42, v115
	v_cvt_pk_bf16_f32 v26, v26, v116
	v_cvt_pk_bf16_f32 v10, v10, v117
	v_cvt_pk_bf16_f32 v59, v59, v118
	v_cvt_pk_bf16_f32 v43, v43, v119
	v_cvt_pk_bf16_f32 v27, v27, v120
	v_cvt_pk_bf16_f32 v11, v11, v121
	v_mul_f32_e32 v60, v60, v76
	v_mul_f32_e32 v44, v44, v76
	v_mul_f32_e32 v28, v28, v76
	v_mul_f32_e32 v12, v12, v76
	v_mul_f32_e32 v61, v61, v77
	v_mul_f32_e32 v45, v45, v77
	v_mul_f32_e32 v29, v29, v77
	v_mul_f32_e32 v13, v13, v77
	v_mov_b32_dpp v114, v60 quad_perm:[1,0,3,2] row_mask:0xf bank_mask:0xf
	v_mov_b32_dpp v115, v44 quad_perm:[1,0,3,2] row_mask:0xf bank_mask:0xf
	v_mov_b32_dpp v116, v28 quad_perm:[1,0,3,2] row_mask:0xf bank_mask:0xf
	v_mov_b32_dpp v117, v12 quad_perm:[1,0,3,2] row_mask:0xf bank_mask:0xf
	v_mov_b32_dpp v118, v61 quad_perm:[1,0,3,2] row_mask:0xf bank_mask:0xf
	v_mov_b32_dpp v119, v45 quad_perm:[1,0,3,2] row_mask:0xf bank_mask:0xf
	v_mov_b32_dpp v120, v29 quad_perm:[1,0,3,2] row_mask:0xf bank_mask:0xf
	v_mov_b32_dpp v121, v13 quad_perm:[1,0,3,2] row_mask:0xf bank_mask:0xf
	v_cvt_pk_bf16_f32 v60, v60, v114
	v_cvt_pk_bf16_f32 v44, v44, v115
	v_cvt_pk_bf16_f32 v28, v28, v116
	v_cvt_pk_bf16_f32 v12, v12, v117
	v_cvt_pk_bf16_f32 v61, v61, v118
	v_cvt_pk_bf16_f32 v45, v45, v119
	v_cvt_pk_bf16_f32 v29, v29, v120
	v_cvt_pk_bf16_f32 v13, v13, v121
	v_mul_f32_e32 v62, v62, v78
	v_mul_f32_e32 v46, v46, v78
	v_mul_f32_e32 v30, v30, v78
	v_mul_f32_e32 v14, v14, v78
	v_mul_f32_e32 v63, v63, v79
	v_mul_f32_e32 v47, v47, v79
	v_mul_f32_e32 v31, v31, v79
	v_mul_f32_e32 v15, v15, v79
	v_mov_b32_dpp v114, v62 quad_perm:[1,0,3,2] row_mask:0xf bank_mask:0xf
	v_mov_b32_dpp v115, v46 quad_perm:[1,0,3,2] row_mask:0xf bank_mask:0xf
	v_mov_b32_dpp v116, v30 quad_perm:[1,0,3,2] row_mask:0xf bank_mask:0xf
	v_mov_b32_dpp v117, v14 quad_perm:[1,0,3,2] row_mask:0xf bank_mask:0xf
	v_mov_b32_dpp v118, v63 quad_perm:[1,0,3,2] row_mask:0xf bank_mask:0xf
	v_mov_b32_dpp v119, v47 quad_perm:[1,0,3,2] row_mask:0xf bank_mask:0xf
	v_mov_b32_dpp v120, v31 quad_perm:[1,0,3,2] row_mask:0xf bank_mask:0xf
	v_mov_b32_dpp v121, v15 quad_perm:[1,0,3,2] row_mask:0xf bank_mask:0xf
	v_cvt_pk_bf16_f32 v62, v62, v114
	v_cvt_pk_bf16_f32 v46, v46, v115
	v_cvt_pk_bf16_f32 v30, v30, v116
	v_cvt_pk_bf16_f32 v14, v14, v117
	v_cvt_pk_bf16_f32 v63, v63, v118
	v_cvt_pk_bf16_f32 v47, v47, v119
	v_cvt_pk_bf16_f32 v31, v31, v120
	v_cvt_pk_bf16_f32 v15, v15, v121
	v_mul_f32_e32 v64, v64, v80
	v_mul_f32_e32 v48, v48, v80
	v_mul_f32_e32 v32, v32, v80
	v_mul_f32_e32 v16, v16, v80
	v_mul_f32_e32 v65, v65, v81
	v_mul_f32_e32 v49, v49, v81
	v_mul_f32_e32 v33, v33, v81
	v_mul_f32_e32 v17, v17, v81
	v_mov_b32_dpp v114, v64 quad_perm:[1,0,3,2] row_mask:0xf bank_mask:0xf
	v_mov_b32_dpp v115, v48 quad_perm:[1,0,3,2] row_mask:0xf bank_mask:0xf
	v_mov_b32_dpp v116, v32 quad_perm:[1,0,3,2] row_mask:0xf bank_mask:0xf
	v_mov_b32_dpp v117, v16 quad_perm:[1,0,3,2] row_mask:0xf bank_mask:0xf
	v_mov_b32_dpp v118, v65 quad_perm:[1,0,3,2] row_mask:0xf bank_mask:0xf
	v_mov_b32_dpp v119, v49 quad_perm:[1,0,3,2] row_mask:0xf bank_mask:0xf
	v_mov_b32_dpp v120, v33 quad_perm:[1,0,3,2] row_mask:0xf bank_mask:0xf
	v_mov_b32_dpp v121, v17 quad_perm:[1,0,3,2] row_mask:0xf bank_mask:0xf
	v_cvt_pk_bf16_f32 v64, v64, v114
	v_cvt_pk_bf16_f32 v48, v48, v115
	v_cvt_pk_bf16_f32 v32, v32, v116
	v_cvt_pk_bf16_f32 v16, v16, v117
	v_cvt_pk_bf16_f32 v65, v65, v118
	v_cvt_pk_bf16_f32 v49, v49, v119
	v_cvt_pk_bf16_f32 v33, v33, v120
	v_cvt_pk_bf16_f32 v17, v17, v121
	s_mov_b64 s[100:101], exec
	s_and_b64 exec, exec, s[6:7]
	ds_write_b32 v83, v50
	ds_write_b32 v83, v34 offset:64
	ds_write_b32 v83, v18 offset:128
	ds_write_b32 v83, v2 offset:192
	ds_write_b32 v83, v51 offset:256
	ds_write_b32 v83, v35 offset:320
	ds_write_b32 v83, v19 offset:384
	ds_write_b32 v83, v3 offset:448
	ds_write_b32 v83, v52 offset:512
	ds_write_b32 v83, v36 offset:576
	ds_write_b32 v83, v20 offset:640
	ds_write_b32 v83, v4 offset:704
	ds_write_b32 v83, v53 offset:768
	ds_write_b32 v83, v37 offset:832
	ds_write_b32 v83, v21 offset:896
	ds_write_b32 v83, v5 offset:960
	ds_write_b32 v83, v54 offset:2048
	ds_write_b32 v83, v38 offset:2112
	ds_write_b32 v83, v22 offset:2176
	ds_write_b32 v83, v6 offset:2240
	ds_write_b32 v83, v55 offset:2304
	ds_write_b32 v83, v39 offset:2368
	ds_write_b32 v83, v23 offset:2432
	ds_write_b32 v83, v7 offset:2496
	ds_write_b32 v83, v56 offset:2560
	ds_write_b32 v83, v40 offset:2624
	ds_write_b32 v83, v24 offset:2688
	ds_write_b32 v83, v8 offset:2752
	ds_write_b32 v83, v57 offset:2816
	ds_write_b32 v83, v41 offset:2880
	ds_write_b32 v83, v25 offset:2944
	ds_write_b32 v83, v9 offset:3008
	ds_write_b32 v83, v58 offset:4096
	ds_write_b32 v83, v42 offset:4160
	ds_write_b32 v83, v26 offset:4224
	ds_write_b32 v83, v10 offset:4288
	ds_write_b32 v83, v59 offset:4352
	ds_write_b32 v83, v43 offset:4416
	ds_write_b32 v83, v27 offset:4480
	ds_write_b32 v83, v11 offset:4544
	ds_write_b32 v83, v60 offset:4608
	ds_write_b32 v83, v44 offset:4672
	ds_write_b32 v83, v28 offset:4736
	ds_write_b32 v83, v12 offset:4800
	ds_write_b32 v83, v61 offset:4864
	ds_write_b32 v83, v45 offset:4928
	ds_write_b32 v83, v29 offset:4992
	ds_write_b32 v83, v13 offset:5056
	ds_write_b32 v83, v62 offset:6144
	ds_write_b32 v83, v46 offset:6208
	ds_write_b32 v83, v30 offset:6272
	ds_write_b32 v83, v14 offset:6336
	ds_write_b32 v83, v63 offset:6400
	ds_write_b32 v83, v47 offset:6464
	ds_write_b32 v83, v31 offset:6528
	ds_write_b32 v83, v15 offset:6592
	ds_write_b32 v83, v64 offset:6656
	ds_write_b32 v83, v48 offset:6720
	ds_write_b32 v83, v32 offset:6784
	ds_write_b32 v83, v16 offset:6848
	ds_write_b32 v83, v65 offset:6912
	ds_write_b32 v83, v49 offset:6976
	ds_write_b32 v83, v33 offset:7040
	ds_write_b32 v83, v17 offset:7104
	s_mov_b64 exec, s[100:101]
	ds_read_b128 v[66:69], v82
	ds_read_b128 v[70:73], v82 offset:1024
	ds_read_b128 v[74:77], v82 offset:2048
	ds_read_b128 v[78:81], v82 offset:3072
	ds_read_b128 v[86:89], v82 offset:4096
	ds_read_b128 v[90:93], v82 offset:5120
	ds_read_b128 v[94:97], v82 offset:6144
	ds_read_b128 v[98:101], v82 offset:7168
	s_waitcnt lgkmcnt(7)
	global_store_dwordx4 v84, v[66:69], s[0:1]
	s_waitcnt lgkmcnt(6)
	v_add_u32_e32 v85, 16384, v84
	global_store_dwordx4 v85, v[70:73], s[0:1]
	s_waitcnt lgkmcnt(5)
	v_add_u32_e32 v85, 32768, v84
	global_store_dwordx4 v85, v[74:77], s[0:1]
	s_waitcnt lgkmcnt(4)
	v_add_u32_e32 v85, 49152, v84
	global_store_dwordx4 v85, v[78:81], s[0:1]
	s_waitcnt lgkmcnt(3)
	v_add_u32_e32 v85, 65536, v84
	global_store_dwordx4 v85, v[86:89], s[0:1]
	s_waitcnt lgkmcnt(2)
	v_add_u32_e32 v85, 81920, v84
	global_store_dwordx4 v85, v[90:93], s[0:1]
	s_waitcnt lgkmcnt(1)
	v_add_u32_e32 v85, 98304, v84
	global_store_dwordx4 v85, v[94:97], s[0:1]
	s_waitcnt lgkmcnt(0)
	v_add_u32_e32 v85, 114688, v84
	global_store_dwordx4 v85, v[98:101], s[0:1]
	s_branch .LBB0_593
